# baseline (speedup 1.0000x reference)
amdhsa.kernels:
  - .agpr_count:     8
    .args:
      - .actual_access:  read_only
        .address_space:  global
        .offset:         0
        .size:           8
        .value_kind:     global_buffer
      - .actual_access:  read_only
        .address_space:  global
        .offset:         8
        .size:           8
        .value_kind:     global_buffer
      - .actual_access:  read_only
        .address_space:  global
        .offset:         16
        .size:           8
        .value_kind:     global_buffer
      - .actual_access:  read_only
        .address_space:  global
        .offset:         24
        .size:           8
        .value_kind:     global_buffer
      - .actual_access:  write_only
        .address_space:  global
        .offset:         32
        .size:           8
        .value_kind:     global_buffer
      - .actual_access:  write_only
        .address_space:  global
        .offset:         40
        .size:           8
        .value_kind:     global_buffer
    .group_segment_fixed_size: 4224
    .kernarg_segment_align: 8
    .kernarg_segment_size: 48
    .language:       OpenCL C
    .language_version:
      - 2
      - 0
    .max_flat_workgroup_size: 128
    .name:           _Z11init_kernelPKfS0_S0_S0_PDF16_S1_
    .private_segment_fixed_size: 0
    .sgpr_count:     22
    .sgpr_spill_count: 0
    .symbol:         _Z11init_kernelPKfS0_S0_S0_PDF16_S1_.kd
    .uniform_work_group_size: 1
    .uses_dynamic_stack: false
    .vgpr_count:     52
    .vgpr_spill_count: 0
    .wavefront_size: 64
  - .agpr_count:     8
    .args:
      - .actual_access:  read_only
        .address_space:  global
        .offset:         0
        .size:           8
        .value_kind:     global_buffer
      - .actual_access:  read_only
        .address_space:  global
        .offset:         8
        .size:           8
        .value_kind:     global_buffer
      - .actual_access:  read_only
        .address_space:  global
        .offset:         16
        .size:           8
        .value_kind:     global_buffer
      - .actual_access:  read_only
        .address_space:  global
        .offset:         24
        .size:           8
        .value_kind:     global_buffer
      - .actual_access:  read_only
        .address_space:  global
        .offset:         32
        .size:           8
        .value_kind:     global_buffer
      - .actual_access:  read_only
        .address_space:  global
        .offset:         40
        .size:           8
        .value_kind:     global_buffer
      - .actual_access:  write_only
        .address_space:  global
        .offset:         48
        .size:           8
        .value_kind:     global_buffer
    .group_segment_fixed_size: 4352
    .kernarg_segment_align: 8
    .kernarg_segment_size: 56
    .language:       OpenCL C
    .language_version:
      - 2
      - 0
    .max_flat_workgroup_size: 128
    .name:           _Z12final_kernelPKDF16_S0_PKfS2_S2_S2_Pf
    .private_segment_fixed_size: 0
    .sgpr_count:     26
    .sgpr_spill_count: 0
    .symbol:         _Z12final_kernelPKDF16_S0_PKfS2_S2_S2_Pf.kd
    .uniform_work_group_size: 1
    .uses_dynamic_stack: false
    .vgpr_count:     60
    .vgpr_spill_count: 0
    .wavefront_size: 64
  - .agpr_count:     0
    .args:
      - .actual_access:  read_only
        .address_space:  global
        .offset:         0
        .size:           8
        .value_kind:     global_buffer
      - .actual_access:  read_only
        .address_space:  global
        .offset:         8
        .size:           8
        .value_kind:     global_buffer
      - .actual_access:  read_only
        .address_space:  global
        .offset:         16
        .size:           8
        .value_kind:     global_buffer
      - .actual_access:  read_only
        .address_space:  global
        .offset:         24
        .size:           8
        .value_kind:     global_buffer
      - .actual_access:  read_only
        .address_space:  global
        .offset:         32
        .size:           8
        .value_kind:     global_buffer
      - .actual_access:  read_only
        .address_space:  global
        .offset:         40
        .size:           8
        .value_kind:     global_buffer
      - .actual_access:  read_only
        .address_space:  global
        .offset:         48
        .size:           8
        .value_kind:     global_buffer
      - .actual_access:  read_only
        .address_space:  global
        .offset:         56
        .size:           8
        .value_kind:     global_buffer
      - .actual_access:  read_only
        .address_space:  global
        .offset:         64
        .size:           8
        .value_kind:     global_buffer
      - .actual_access:  read_only
        .address_space:  global
        .offset:         72
        .size:           8
        .value_kind:     global_buffer
      - .address_space:  global
        .offset:         80
        .size:           8
        .value_kind:     global_buffer
    .group_segment_fixed_size: 16896
    .kernarg_segment_align: 8
    .kernarg_segment_size: 88
    .language:       OpenCL C
    .language_version:
      - 2
      - 0
    .max_flat_workgroup_size: 128
    .name:           _Z11edge_kernelILi36ELb1EEvPKfS1_PKDF16_PKiS5_S1_S1_S1_S1_S1_PDF16_
    .private_segment_fixed_size: 0
    .sgpr_count:     45
    .sgpr_spill_count: 0
    .symbol:         _Z11edge_kernelILi36ELb1EEvPKfS1_PKDF16_PKiS5_S1_S1_S1_S1_S1_PDF16_.kd
    .uniform_work_group_size: 1
    .uses_dynamic_stack: false
    .vgpr_count:     168
    .vgpr_spill_count: 0
    .wavefront_size: 64
  - .agpr_count:     0
    .args:
      - .actual_access:  read_only
        .address_space:  global
        .offset:         0
        .size:           8
        .value_kind:     global_buffer
      - .actual_access:  read_only
        .address_space:  global
        .offset:         8
        .size:           8
        .value_kind:     global_buffer
      - .actual_access:  read_only
        .address_space:  global
        .offset:         16
        .size:           8
        .value_kind:     global_buffer
      - .actual_access:  read_only
        .address_space:  global
        .offset:         24
        .size:           8
        .value_kind:     global_buffer
      - .actual_access:  read_only
        .address_space:  global
        .offset:         32
        .size:           8
        .value_kind:     global_buffer
      - .actual_access:  read_only
        .address_space:  global
        .offset:         40
        .size:           8
        .value_kind:     global_buffer
      - .actual_access:  read_only
        .address_space:  global
        .offset:         48
        .size:           8
        .value_kind:     global_buffer
      - .actual_access:  read_only
        .address_space:  global
        .offset:         56
        .size:           8
        .value_kind:     global_buffer
      - .actual_access:  read_only
        .address_space:  global
        .offset:         64
        .size:           8
        .value_kind:     global_buffer
      - .actual_access:  read_only
        .address_space:  global
        .offset:         72
        .size:           8
        .value_kind:     global_buffer
      - .address_space:  global
        .offset:         80
        .size:           8
        .value_kind:     global_buffer
    .group_segment_fixed_size: 16896
    .kernarg_segment_align: 8
    .kernarg_segment_size: 88
    .language:       OpenCL C
    .language_version:
      - 2
      - 0
    .max_flat_workgroup_size: 128
    .name:           _Z11edge_kernelILi64ELb0EEvPKfS1_PKDF16_PKiS5_S1_S1_S1_S1_S1_PDF16_
    .private_segment_fixed_size: 0
    .sgpr_count:     44
    .sgpr_spill_count: 0
    .symbol:         _Z11edge_kernelILi64ELb0EEvPKfS1_PKDF16_PKiS5_S1_S1_S1_S1_S1_PDF16_.kd
    .uniform_work_group_size: 1
    .uses_dynamic_stack: false
    .vgpr_count:     168
    .vgpr_spill_count: 0
    .wavefront_size: 64
